# attention loop head aligned to 256 bytes (was 64)
# speedup vs baseline: 1.0130x; 1.0130x over previous
; __device__ __forceinline__ void lds_barrier() { asm volatile("s_waitcnt lgkmcnt(0)" ::: "memory"); __builtin_amdgcn_s_barrier(); asm volatile("" ::: "memory"); }
; #define AT_LOADK(t) do { const int kr_ = AT_KROW(t); _Pragma("unroll") for (int i_ = 0; i_ < 2; ++i_) kreg[i_] = *(const u32x4*)(Kp + (size_t)(kr_ + prow0 + 32 * i_) * 512 + pch * 8); } while (0)
; #define AT_LOADV(t) do { const int kr_ = AT_KROW(t); _Pragma("unroll") for (int i_ = 0; i_ < 2; ++i_) vreg[i_] = *(const u32x4*)(Vp + (size_t)(kr_ + prow0 + 32 * i_) * 512 + pch * 8); } while (0)
; #define AT_STOREK(st) do { _Pragma("unroll") for (int i_ = 0; i_ < 2; ++i_) *(LAS u32x4*)(L + AT_K + (st) * AT_KBYTES + (prow0 + 32 * i_) * AT_KSTR + pch * 16) = kreg[i_]; } while (0)
; #define AT_STOREV(st) do { _Pragma("unroll") for (int i_ = 0; i_ < 2; ++i_) *(LAS u32x4*)(L + AT_V + (st) * AT_VBYTES + (prow0 + 32 * i_) * AT_VSTR + pch * 16) = vreg[i_]; } while (0)
; __device__ __forceinline__ void attn_unit(const Frame& F, int layer, int qrow0, int ntiles, int b, int head, float lam, float m2, float lam_init) {
;     ...
;     if (wave >= 4) __builtin_amdgcn_s_setprio(1);
;     AT_LOADK(0); AT_LOADV(0); AT_STOREK(0); AT_STOREV(0);
;     if (ntiles > 1) { AT_LOADK(1); AT_STOREK(1); }
;     __syncthreads();
;     f32x16 sa, sb, na, nb;
;     AT_QK(sa, sb, 0);
;     lds_barrier();
;     for (int t = 0; t < ntiles; ++t) {
.Latt_lead0:
	s_nop 7
	s_nop 7
	.p2align 8
